# baseline (speedup 1.0000x reference)
_Z11attn_kernelPKDF16_S0_PDF16_P15HIP_vector_typeIfLj2EE:
	s_lshl_b32 s40, s3, 4
	s_add_u32 s40, s40, s2
	s_lshl_b32 s41, s4, 6
	s_add_u32 s40, s40, s41
	s_and_b32 s41, s40, 7
	s_lshr_b32 s40, s40, 3
	s_and_b32 s2, s41, 3
	s_lshl_b32 s2, s2, 2
	s_and_b32 s3, s40, 3
	s_or_b32 s2, s2, s3
	s_lshr_b32 s3, s40, 2
	s_and_b32 s3, s3, 3
	s_lshr_b32 s4, s41, 2
	s_lshl_b32 s4, s4, 1
	s_lshr_b32 s40, s40, 4
	s_or_b32 s4, s4, s40
	s_and_b32 s40, s2, 3
.Lmy_stag:
	s_cmp_eq_u32 s40, 0
	s_cbranch_scc1 .Lmy_stag_done
	s_sleep 2
	s_sub_u32 s40, s40, 1
	s_branch .Lmy_stag
.Lmy_stag_done:
	s_getpc_b64 s[38:39]
	v_lshlrev_b32_e32 v240, 7, v0
	v_min_u32_e32 v240, 0x3380, v240
	global_load_dword v241, v240, s[38:39]
	s_mov_b32 s5, 0
	s_mov_b32 s28, s3
	s_load_dwordx8 s[20:27], s[0:1], 0x0
	s_mov_b32 s3, s5
	s_lshl_b64 s[0:1], s[4:5], 12
	s_lshl_b64 s[2:3], s[2:3], 8
	s_add_u32 s0, s0, s2
	v_lshrrev_b32_e32 v1, 6, v0
	s_addc_u32 s1, s1, s3
	v_and_b32_e32 v160, 31, v0
	s_lshl_b64 s[2:3], s[0:1], 8
	v_lshlrev_b32_e32 v162, 5, v1
	s_waitcnt lgkmcnt(0)
	s_add_u32 s2, s20, s2
	v_or_b32_e32 v2, v162, v160
	v_bfe_u32 v54, v0, 5, 1
	s_addc_u32 s3, s21, s3
	v_and_b32_e32 v164, 63, v0
	v_lshrrev_b32_e32 v165, 4, v164
	v_add_u32_e32 v165, v162, v165
	v_lshlrev_b32_e32 v165, 8, v165
	v_and_b32_e32 v164, 15, v164
	v_lshl_add_u32 v164, v164, 4, v165
	v_mov_b32_e32 v165, 0
	v_lshl_add_u64 v[2:3], s[2:3], 0, v[164:165]
	s_mov_b64 s[6:7], 0x1000
	v_lshl_add_u64 v[4:5], v[2:3], 0, s[6:7]
	global_load_dwordx4 v[156:159], v[2:3], off
	global_load_dwordx4 v[152:155], v[2:3], off offset:1024
	global_load_dwordx4 v[148:151], v[2:3], off offset:2048
	global_load_dwordx4 v[144:147], v[2:3], off offset:3072
	global_load_dwordx4 v[140:143], v[4:5], off
	global_load_dwordx4 v[136:139], v[4:5], off offset:1024
	global_load_dwordx4 v[132:135], v[4:5], off offset:2048
	global_load_dwordx4 v[128:131], v[4:5], off offset:3072
	v_lshlrev_b32_e32 v164, 4, v54
	s_ashr_i32 s29, s28, 31
	v_bfe_u32 v55, v0, 2, 3
	s_lshl_b64 s[2:3], s[4:5], 20
	s_lshl_b64 s[20:21], s[28:29], 18
	v_lshl_or_b32 v2, v1, 3, v55
	s_add_u32 s4, s22, s2
	v_lshrrev_b32_e32 v3, 2, v2
	s_addc_u32 s7, s23, s3
	v_xor_b32_e32 v4, v3, v0
	s_add_u32 s6, s4, s20
	v_and_b32_e32 v5, 32, v0
	v_lshlrev_b32_e32 v4, 3, v4
	v_lshlrev_b32_e32 v1, 11, v1
	s_addc_u32 s7, s7, s21
	v_lshlrev_b32_e32 v164, 8, v2
	v_and_or_b32 v4, v4, 24, v5
	v_add_u32_e32 v173, 0, v1
	v_lshl_add_u64 v[2:3], s[6:7], 0, v[164:165]
	v_lshlrev_b32_e32 v164, 1, v4
	v_readfirstlane_b32 s4, v173
	v_add_u32_e32 v6, 0x400, v173
	v_lshl_add_u64 v[2:3], v[2:3], 0, v[164:165]
	s_mov_b64 s[6:7], 0x80
	s_mov_b32 m0, s4
	v_readfirstlane_b32 s4, v6
	v_add_u32_e32 v6, 0x4000, v173
	v_lshl_add_u64 v[4:5], v[2:3], 0, s[6:7]
	global_load_lds_dwordx4 v[2:3], off
	s_mov_b32 m0, s4
	s_mov_b64 s[6:7], 0x4000
	v_readfirstlane_b32 s4, v6
	global_load_lds_dwordx4 v[4:5], off
	v_lshl_add_u64 v[4:5], v[2:3], 0, s[6:7]
	s_mov_b32 m0, s4
	s_mov_b64 s[6:7], 0x4080
	global_load_lds_dwordx4 v[4:5], off
	v_add_u32_e32 v4, 0x4400, v173
	v_lshl_add_u64 v[2:3], v[2:3], 0, s[6:7]
	v_readfirstlane_b32 s4, v4
	s_mov_b32 m0, s4
	s_movk_i32 s4, 0x1c0
	global_load_lds_dwordx4 v[2:3], off
	v_lshlrev_b32_e32 v2, 8, v0
	v_and_b32_e32 v2, 0x1800, v2
	v_lshlrev_b32_e32 v3, 6, v0
	v_and_or_b32 v6, v3, s4, v2
	v_xor_b32_e32 v2, v54, v55
	v_lshlrev_b32_e32 v2, 4, v2
	v_and_or_b32 v175, v2, 48, v6
	v_and_b32_e32 v190, 63, v0
	v_lshrrev_b32_e32 v191, 4, v190
	v_and_b32_e32 v192, 15, v190
	v_xor_b32_e32 v193, v192, v191
	v_lshlrev_b32_e32 v193, 4, v193
	v_add_u32_e32 v194, v162, v191
	v_lshlrev_b32_e32 v194, 8, v194
	v_add_u32_e32 v194, 0x10000, v194
	v_and_b32_e32 v195, 15, v160
	v_xor_b32_e32 v195, v195, v54
	v_lshlrev_b32_e32 v195, 4, v195
	v_add_u32_e32 v196, v162, v160
	v_lshlrev_b32_e32 v196, 8, v196
	v_add_u32_e32 v196, 0x10000, v196
	s_waitcnt vmcnt(4)
	v_xor_b32_e32 v197, 0x0, v193
	v_add_u32_e32 v197, v197, v194
	ds_write_b128 v197, v[156:159] offset:0
	v_xor_b32_e32 v197, 0x40, v193
	v_add_u32_e32 v197, v197, v194
	ds_write_b128 v197, v[152:155] offset:1024
	v_xor_b32_e32 v197, 0x80, v193
	v_add_u32_e32 v197, v197, v194
	ds_write_b128 v197, v[148:151] offset:2048
	v_xor_b32_e32 v197, 0xc0, v193
	v_add_u32_e32 v197, v197, v194
	ds_write_b128 v197, v[144:147] offset:3072
	v_xor_b32_e32 v197, 0x0, v193
	v_add_u32_e32 v197, v197, v194
	ds_write_b128 v197, v[140:143] offset:4096
	v_xor_b32_e32 v197, 0x40, v193
	v_add_u32_e32 v197, v197, v194
	ds_write_b128 v197, v[136:139] offset:5120
	v_xor_b32_e32 v197, 0x80, v193
	v_add_u32_e32 v197, v197, v194
	ds_write_b128 v197, v[132:135] offset:6144
	v_xor_b32_e32 v197, 0xc0, v193
	v_add_u32_e32 v197, v197, v194
	ds_write_b128 v197, v[128:131] offset:7168
	s_waitcnt lgkmcnt(0)
	v_xor_b32_e32 v198, 0x0, v195
	v_add_u32_e32 v198, v198, v196
	ds_read_b128 v[156:159], v198
	v_xor_b32_e32 v198, 0x20, v195
	v_add_u32_e32 v198, v198, v196
	ds_read_b128 v[152:155], v198
	v_xor_b32_e32 v198, 0x40, v195
	v_add_u32_e32 v198, v198, v196
	ds_read_b128 v[148:151], v198
	v_xor_b32_e32 v198, 0x60, v195
	v_add_u32_e32 v198, v198, v196
	ds_read_b128 v[144:147], v198
	v_xor_b32_e32 v198, 0x80, v195
	v_add_u32_e32 v198, v198, v196
	ds_read_b128 v[140:143], v198
	v_xor_b32_e32 v198, 0xa0, v195
	v_add_u32_e32 v198, v198, v196
	ds_read_b128 v[136:139], v198
	v_xor_b32_e32 v198, 0xc0, v195
	v_add_u32_e32 v198, v198, v196
	ds_read_b128 v[132:135], v198
	v_xor_b32_e32 v198, 0xe0, v195
	v_add_u32_e32 v198, v198, v196
	ds_read_b128 v[128:131], v198
	s_waitcnt vmcnt(2)
	v_add_u32_e32 v172, 0, v175
	s_waitcnt lgkmcnt(0)
	s_barrier
	ds_read_b128 v[2:5], v172
	ds_read_b128 v[34:37], v172 offset:512
	v_bitop3_b32 v7, v54, v55, 2 bitop3:0x36
	v_lshlrev_b32_e32 v7, 4, v7
	v_and_or_b32 v176, v7, 48, v6
	v_add_u32_e32 v174, 0, v176
	ds_read_b128 v[18:21], v174
	ds_read_b128 v[38:41], v174 offset:512
	s_mov_b32 s33, 0x41200000
	s_cmp_lg_u32 0, -1
	s_cselect_b32 s37, 0, 0
	s_waitcnt vmcnt(2) lgkmcnt(0)
	v_mfma_f32_32x32x16_f16 v[2:17], v[2:5], v[156:159], 0
	s_movk_i32 s4, 0x110
	v_and_b32_e32 v161, 63, v0
	v_lshl_or_b32 v1, v55, 8, v1
	s_mov_b32 s18, s5
	s_mov_b32 s19, s5
	s_mov_b32 s6, s5
	s_mov_b32 s7, s5
	v_mfma_f32_32x32x16_f16 v[2:17], v[18:21], v[152:155], v[2:17]
	ds_read_b128 v[18:21], v172 offset:8192
	ds_read_b128 v[42:45], v172 offset:8704
	ds_read_b128 v[46:49], v174 offset:8192
	ds_read_b128 v[50:53], v174 offset:8704
	s_mov_b32 s8, s5
	s_mov_b32 s9, s5
	s_mov_b32 s10, s5
	s_mov_b32 s11, s5
	s_mov_b32 s12, s5
	s_waitcnt lgkmcnt(3)
	v_mfma_f32_32x32x16_f16 v[18:33], v[18:21], v[156:159], 0
	s_mov_b32 s13, s5
	s_mov_b32 s14, s5
	s_mov_b32 s15, s5
	s_mov_b32 s16, s5
	s_mov_b32 s17, s5
	s_mov_b32 s36, 1
	s_mov_b32 s34, -1
	s_waitcnt lgkmcnt(1)
	v_mfma_f32_32x32x16_f16 v[18:33], v[46:49], v[152:155], v[18:33]
	s_mov_b32 s35, 2
	s_mov_b64 s[30:31], 0x8000
	v_mfma_f32_32x32x16_f16 v[2:17], v[34:37], v[148:151], v[2:17]
	v_mfma_f32_32x32x16_f16 v[18:33], v[42:45], v[148:151], v[18:33]
	v_mfma_f32_32x32x16_f16 v[2:17], v[38:41], v[144:147], v[2:17]
	ds_read_b128 v[34:37], v172 offset:1024
	ds_read_b128 v[38:41], v172 offset:1536
	s_waitcnt lgkmcnt(2)
	v_mfma_f32_32x32x16_f16 v[18:33], v[50:53], v[144:147], v[18:33]
	s_waitcnt lgkmcnt(1)
	v_mfma_f32_32x32x16_f16 v[2:17], v[34:37], v[140:143], v[2:17]
	ds_read_b128 v[34:37], v172 offset:9216
	ds_read_b128 v[42:45], v172 offset:9728
	s_waitcnt lgkmcnt(1)
	v_mfma_f32_32x32x16_f16 v[18:33], v[34:37], v[140:143], v[18:33]
	ds_read_b128 v[34:37], v174 offset:1024
	ds_read_b128 v[46:49], v174 offset:1536
	s_waitcnt lgkmcnt(1)
	v_mfma_f32_32x32x16_f16 v[2:17], v[34:37], v[136:139], v[2:17]
	ds_read_b128 v[34:37], v174 offset:9216
	ds_read_b128 v[50:53], v174 offset:9728
	v_mfma_f32_32x32x16_f16 v[2:17], v[38:41], v[132:135], v[2:17]
	s_waitcnt lgkmcnt(1)
	v_mfma_f32_32x32x16_f16 v[18:33], v[34:37], v[136:139], v[18:33]
	v_mov_b32_e32 v34, 0xf149f2ca
	v_mfma_f32_32x32x16_f16 v[2:17], v[46:49], v[128:131], v[2:17]
	v_mfma_f32_32x32x16_f16 v[18:33], v[42:45], v[132:135], v[18:33]
	s_nop 10
	v_max_f32_e32 v35, v3, v3
	v_max_f32_e32 v36, v2, v2
	v_max_f32_e32 v35, v36, v35
	v_max3_f32 v35, v35, v4, v5
	v_max3_f32 v35, v35, v6, v7
	v_max3_f32 v35, v35, v8, v9
	v_max3_f32 v35, v35, v10, v11
	s_waitcnt lgkmcnt(0)
	v_mfma_f32_32x32x16_f16 v[18:33], v[50:53], v[128:131], v[18:33]
	v_max3_f32 v35, v35, v12, v13
	v_max3_f32 v35, v35, v14, v15
	v_max3_f32 v35, v35, v16, v17
	s_nop 8
	v_max3_f32 v35, v35, v18, v19
	v_max3_f32 v35, v35, v20, v21
	v_max3_f32 v35, v35, v22, v23
	v_max3_f32 v35, v35, v24, v25
	v_max3_f32 v35, v35, v26, v27
	v_max3_f32 v35, v35, v28, v29
	v_max3_f32 v35, v35, v30, v31
	v_max3_f32 v35, v35, v32, v33
	v_mov_b32_e32 v36, v35
	s_nop 1
	v_permlane32_swap_b32_e32 v35, v36
	v_max_f32_e32 v36, v36, v36
	v_max_f32_e32 v35, v35, v35
	v_max_f32_e32 v35, v35, v36
	v_add_f32_e32 v36, 0x7149f2ca, v35
	v_cmp_ge_f32_e32 vcc, s33, v36
	s_cmp_eq_u64 vcc, exec
	v_max_f32_e32 v35, 0xf149f2ca, v35
	s_cselect_b64 vcc, -1, 0
	v_cndmask_b32_e32 v168, v35, v34, vcc
	v_sub_f32_e32 v96, v18, v168
	v_sub_f32_e32 v97, v19, v168
	v_lshlrev_b32_e32 v18, 4, v0
	v_lshrrev_b32_e32 v19, 4, v0
	v_sub_f32_e32 v98, v20, v168
	v_and_b32_e32 v18, 0xc0, v18
	v_bitop3_b32 v19, v19, v54, 1 bitop3:0x6c
	v_lshlrev_b32_e32 v20, 3, v0
	v_sub_f32_e32 v99, v21, v168
	v_lshl_or_b32 v18, v54, 11, v18
	v_lshlrev_b32_e32 v19, 5, v19
	v_and_b32_e32 v21, 8, v20
	v_or3_b32 v18, v18, v21, v19
	v_and_b32_e32 v19, 16, v20
	v_sub_f32_e32 v0, 0xf149f2ca, v35
	v_add3_u32 v163, v19, s37, v18
	v_bitop3_b32 v169, v18, s4, v19 bitop3:0x36
	v_exp_f32_e32 v18, v0
	s_add_u32 s2, s2, s20
	v_sub_f32_e32 v2, v2, v168
	v_sub_f32_e32 v3, v3, v168
	v_sub_f32_e32 v4, v4, v168
	v_sub_f32_e32 v5, v5, v168
	v_sub_f32_e32 v6, v6, v168
	v_sub_f32_e32 v7, v7, v168
	v_sub_f32_e32 v8, v8, v168
	v_sub_f32_e32 v9, v9, v168
	v_sub_f32_e32 v10, v10, v168
	v_sub_f32_e32 v11, v11, v168
	v_sub_f32_e32 v12, v12, v168
	v_sub_f32_e32 v13, v13, v168
	v_sub_f32_e32 v14, v14, v168
	v_sub_f32_e32 v15, v15, v168
	v_sub_f32_e32 v16, v16, v168
	v_sub_f32_e32 v17, v17, v168
	s_addc_u32 s3, s3, s21
	s_mov_b32 s4, s5
	v_exp_f32_e32 v127, v2
	v_exp_f32_e32 v180, v3
	v_exp_f32_e32 v125, v4
	v_exp_f32_e32 v179, v5
	v_exp_f32_e32 v123, v6
	v_exp_f32_e32 v126, v7
	v_exp_f32_e32 v122, v8
	v_exp_f32_e32 v124, v9
	v_exp_f32_e32 v119, v10
	v_exp_f32_e32 v121, v11
	v_exp_f32_e32 v117, v12
	v_exp_f32_e32 v120, v13
	v_exp_f32_e32 v115, v14
	v_exp_f32_e32 v118, v15
	v_exp_f32_e32 v114, v16
	v_exp_f32_e32 v116, v17
	v_or3_b32 v0, s2, v1, v164
	v_mov_b32_e32 v1, s3
	v_lshlrev_b32_e32 v164, 3, v54
	v_mov_b64_e32 v[62:63], s[18:19]
	v_lshl_add_u64 v[0:1], s[22:23], 0, v[0:1]
	s_mov_b64 s[2:3], 0xc080
	v_mov_b64_e32 v[48:49], s[4:5]
	v_sub_f32_e32 v100, v22, v168
	v_sub_f32_e32 v101, v23, v168
	v_sub_f32_e32 v102, v24, v168
	v_sub_f32_e32 v103, v25, v168
	v_sub_f32_e32 v104, v26, v168
	v_sub_f32_e32 v105, v27, v168
	v_sub_f32_e32 v106, v28, v168
	v_sub_f32_e32 v107, v29, v168
	v_sub_f32_e32 v108, v30, v168
	v_sub_f32_e32 v109, v31, v168
	v_sub_f32_e32 v110, v32, v168
	v_sub_f32_e32 v111, v33, v168
	v_lshl_add_u64 v[170:171], v[0:1], 0, s[2:3]
	s_movk_i32 s2, 0xbf80
	s_movk_i32 s20, 0xc000
	s_movk_i32 s22, 0xff80
	v_mov_b32_e32 v166, 1.0
	v_mov_b64_e32 v[60:61], s[16:17]
	v_mov_b64_e32 v[58:59], s[14:15]
	v_mov_b64_e32 v[56:57], s[12:13]
	v_mov_b64_e32 v[54:55], s[10:11]
	v_mov_b64_e32 v[52:53], s[8:9]
	v_mov_b64_e32 v[50:51], s[6:7]
	v_mov_b64_e32 v[32:33], v[48:49]
	v_mov_b64_e32 v[16:17], v[48:49]
	v_mov_b64_e32 v[0:1], v[48:49]
	s_mov_b32 s3, -1
	s_mov_b32 s21, -1
	s_mov_b32 s23, -1
	v_add_u32_e32 v167, s37, v169
	v_mov_b64_e32 v[34:35], v[50:51]
	v_mov_b64_e32 v[36:37], v[52:53]
	v_mov_b64_e32 v[38:39], v[54:55]
	v_mov_b64_e32 v[40:41], v[56:57]
	v_mov_b64_e32 v[42:43], v[58:59]
	v_mov_b64_e32 v[44:45], v[60:61]
	v_mov_b64_e32 v[46:47], v[62:63]
	v_mov_b64_e32 v[18:19], v[50:51]
	v_mov_b64_e32 v[20:21], v[52:53]
	v_mov_b64_e32 v[22:23], v[54:55]
	v_mov_b64_e32 v[24:25], v[56:57]
	v_mov_b64_e32 v[26:27], v[58:59]
	v_mov_b64_e32 v[28:29], v[60:61]
	v_mov_b64_e32 v[30:31], v[62:63]
	v_mov_b64_e32 v[2:3], v[50:51]
	v_mov_b64_e32 v[4:5], v[52:53]
	v_mov_b64_e32 v[6:7], v[54:55]
	v_mov_b64_e32 v[8:9], v[56:57]
	v_mov_b64_e32 v[10:11], v[58:59]
	v_mov_b64_e32 v[12:13], v[60:61]
	v_mov_b64_e32 v[14:15], v[62:63]
